# late_prep: cold f32 weight streams (w_proj, w_out transposers, peer_v rows) loaded with nt policy
# speedup vs baseline: 1.0042x; 1.0042x over previous
; #define LAS __attribute__((address_space(3)))
; template <int FP8> __device__ __forceinline__ void transpose_stream(const float* W, int K, int N, void* WT_, int split, int add, int ldt, int col_add, LAS float* scr, int it0, int its, int nitems, int lane, const float* kscale) {
;     const int nblk = N / 32; float cur[32];
;     if (it0 < nitems) { const int kb = it0 / nblk, nb = it0 % nblk;
; #pragma unroll
;         for (int i = 0; i < 32; ++i) cur[i] = W[(size_t)(64 * kb + 2 * i + (lane >> 5)) * N + 32 * nb + (lane & 31)]; }
; __device__ __forceinline__ void late_prep(Frame& F, int mgw, int mngw) {
;     LAS float* scr = (LAS float*)(F.lds + F.wave * 16384);
;     constexpr int I_PA = (RW / 64) * (D_ / 32), I_OUT = (D_ / 64) * (D_ / 32), I_Q = (D_ / 64) * (2048 / 32);
;     transpose_stream<true>(F.in[14], RW, D_, F.ws + WS_WPA, 1 << 30, 0, 4096, 0, scr, mgw, mngw, I_PA, F.lane, nullptr);
.LBB0_2037:
	s_lshl_b32 s0, s66, 14
	s_add_i32 s8, s94, 0xfffffc00
	s_add_i32 s10, s34, 0xfffffc00
	s_add_i32 s3, s0, 0
	s_cmpk_lt_i32 s8, 0x1000
	s_cselect_b64 s[4:5], -1, 0
	s_cmpk_gt_i32 s8, 0xfff
	s_waitcnt vmcnt(11)
	v_ashrrev_i32_e32 v2, 5, v148
	v_and_b32_e32 v4, 31, v148
	v_ashrrev_i32_e32 v3, 2, v148
	v_lshlrev_b32_e32 v76, 4, v148
	v_and_b32_e32 v5, -4, v148
	s_barrier
	s_cbranch_scc1 .LBB0_2050
	s_ashr_i32 s0, s8, 31
	s_lshr_b32 s0, s0, 25
	s_add_i32 s0, s8, s0
	s_and_b32 s1, s0, 0x7ffff80
	s_sub_i32 s1, s8, s1
	s_ashr_i32 s0, s0, 7
	v_readlane_b32 s40, v254, 2
	s_waitcnt vmcnt(10)
	v_lshl_add_u32 v6, s0, 6, v2
	s_lshl_b32 s0, s1, 5
	v_readlane_b32 s44, v254, 6
	v_readlane_b32 s45, v254, 7
	v_readlane_b32 s46, v254, 8
	v_readlane_b32 s47, v254, 9
	v_readlane_b32 s48, v254, 10
	v_readlane_b32 s49, v254, 11
	v_readlane_b32 s50, v254, 12
	v_readlane_b32 s51, v254, 13
	s_ashr_i32 s1, s0, 31
	v_readlane_b32 s52, v254, 14
	v_readlane_b32 s53, v254, 15
	v_readlane_b32 s54, v254, 16
	v_readlane_b32 s55, v254, 17
	s_mov_b64 s[44:45], s[48:49]
	s_lshl_b64 s[0:1], s[0:1], 2
	s_mov_b64 s[46:47], s[50:51]
	s_mov_b64 s[48:49], s[52:53]
	s_add_u32 s6, s48, s0
	v_mov_b32_e32 v71, 0
	s_addc_u32 s7, s49, s1
	v_lshlrev_b32_e32 v70, 2, v4
	v_ashrrev_i32_e32 v7, 31, v6
	v_lshl_add_u64 v[72:73], s[6:7], 0, v[70:71]
	v_lshlrev_b64 v[6:7], 14, v[6:7]
	s_mov_b64 s[6:7], 0x8000
	v_lshl_add_u64 v[8:9], v[6:7], 0, s[6:7]
	s_mov_b64 s[6:7], 0x10000
	s_waitcnt vmcnt(9)
	v_lshl_add_u64 v[10:11], v[6:7], 0, s[6:7]
	s_mov_b64 s[6:7], 0x18000
	v_lshl_add_u64 v[12:13], v[6:7], 0, s[6:7]
	s_mov_b64 s[6:7], 0x20000
	s_waitcnt vmcnt(8)
	v_lshl_add_u64 v[14:15], v[6:7], 0, s[6:7]
	s_mov_b64 s[6:7], 0x28000
	v_lshl_add_u64 v[16:17], v[6:7], 0, s[6:7]
	s_mov_b64 s[6:7], 0x30000
	s_waitcnt vmcnt(7)
	v_lshl_add_u64 v[18:19], v[6:7], 0, s[6:7]
	s_mov_b64 s[6:7], 0x38000
	s_waitcnt vmcnt(6)
	v_lshl_add_u64 v[22:23], v[72:73], 0, v[6:7]
	v_lshl_add_u64 v[20:21], v[6:7], 0, s[6:7]
	s_mov_b64 s[6:7], 0x40000
	v_lshl_add_u64 v[24:25], v[72:73], 0, v[8:9]
	s_waitcnt vmcnt(5)
	v_lshl_add_u64 v[26:27], v[72:73], 0, v[10:11]
	v_lshl_add_u64 v[28:29], v[72:73], 0, v[12:13]
	s_waitcnt vmcnt(4)
	v_lshl_add_u64 v[30:31], v[72:73], 0, v[14:15]
	v_lshl_add_u64 v[32:33], v[72:73], 0, v[16:17]
	s_waitcnt vmcnt(3)
	v_lshl_add_u64 v[34:35], v[72:73], 0, v[18:19]
	v_lshl_add_u64 v[36:37], v[72:73], 0, v[20:21]
	global_load_dword v86, v[22:23], off nt
	global_load_dword v85, v[24:25], off nt
	global_load_dword v84, v[26:27], off nt
	global_load_dword v83, v[28:29], off nt
	global_load_dword v82, v[30:31], off nt
	global_load_dword v81, v[32:33], off nt
	global_load_dword v80, v[34:35], off nt
	global_load_dword v79, v[36:37], off nt
	v_lshl_add_u64 v[22:23], v[6:7], 0, s[6:7]
	s_mov_b64 s[6:7], 0x48000
	v_lshl_add_u64 v[24:25], v[6:7], 0, s[6:7]
	s_mov_b64 s[6:7], 0x50000
	v_lshl_add_u64 v[26:27], v[6:7], 0, s[6:7]
	s_mov_b64 s[6:7], 0x58000
	v_lshl_add_u64 v[28:29], v[6:7], 0, s[6:7]
	s_mov_b64 s[6:7], 0x60000
	v_lshl_add_u64 v[30:31], v[6:7], 0, s[6:7]
	s_mov_b64 s[6:7], 0x68000
	v_lshl_add_u64 v[32:33], v[6:7], 0, s[6:7]
	s_mov_b64 s[6:7], 0x70000
	v_lshl_add_u64 v[34:35], v[6:7], 0, s[6:7]
	s_mov_b64 s[6:7], 0x78000
	s_waitcnt vmcnt(10)
	v_lshl_add_u64 v[38:39], v[72:73], 0, v[22:23]
	v_lshl_add_u64 v[36:37], v[6:7], 0, s[6:7]
	s_mov_b64 s[6:7], 0x80000
	v_lshl_add_u64 v[40:41], v[72:73], 0, v[24:25]
	s_waitcnt vmcnt(9)
	v_lshl_add_u64 v[42:43], v[72:73], 0, v[26:27]
	v_lshl_add_u64 v[44:45], v[72:73], 0, v[28:29]
	s_waitcnt vmcnt(8)
; template <int FP8> __device__ __forceinline__ void transpose_stream(const float* W, int K, int N, void* WT_, int split, int add, int ldt, int col_add, LAS float* scr, int it0, int its, int nitems, int lane, const float* kscale) {
;     const int nblk = N / 32; float cur[32];
;     if (it0 < nitems) { const int kb = it0 / nblk, nb = it0 % nblk;
; #pragma unroll
;         for (int i = 0; i < 32; ++i) cur[i] = W[(size_t)(64 * kb + 2 * i + (lane >> 5)) * N + 32 * nb + (lane & 31)]; }
	v_lshl_add_u64 v[46:47], v[72:73], 0, v[30:31]
	v_lshl_add_u64 v[48:49], v[72:73], 0, v[32:33]
	v_lshl_add_u64 v[50:51], v[72:73], 0, v[34:35]
	v_lshl_add_u64 v[52:53], v[72:73], 0, v[36:37]
	global_load_dword v94, v[38:39], off nt
	global_load_dword v93, v[40:41], off nt
	global_load_dword v92, v[42:43], off nt
	global_load_dword v91, v[44:45], off nt
	global_load_dword v90, v[46:47], off nt
	global_load_dword v89, v[48:49], off nt
	global_load_dword v88, v[50:51], off nt
	global_load_dword v87, v[52:53], off nt
	v_lshl_add_u64 v[38:39], v[6:7], 0, s[6:7]
	s_mov_b64 s[6:7], 0x88000
	v_lshl_add_u64 v[40:41], v[6:7], 0, s[6:7]
	s_mov_b64 s[6:7], 0x90000
	v_lshl_add_u64 v[42:43], v[6:7], 0, s[6:7]
	s_mov_b64 s[6:7], 0x98000
	v_lshl_add_u64 v[44:45], v[6:7], 0, s[6:7]
	s_mov_b64 s[6:7], 0xa0000
	v_lshl_add_u64 v[46:47], v[6:7], 0, s[6:7]
	s_mov_b64 s[6:7], 0xa8000
	v_lshl_add_u64 v[48:49], v[6:7], 0, s[6:7]
	s_mov_b64 s[6:7], 0xb0000
	v_lshl_add_u64 v[50:51], v[6:7], 0, s[6:7]
	s_mov_b64 s[6:7], 0xb8000
	v_lshl_add_u64 v[54:55], v[72:73], 0, v[38:39]
	v_lshl_add_u64 v[52:53], v[6:7], 0, s[6:7]
	s_mov_b64 s[6:7], 0xc0000
	v_lshl_add_u64 v[56:57], v[72:73], 0, v[40:41]
	v_lshl_add_u64 v[58:59], v[72:73], 0, v[42:43]
	v_lshl_add_u64 v[60:61], v[72:73], 0, v[44:45]
	v_lshl_add_u64 v[62:63], v[72:73], 0, v[46:47]
	v_lshl_add_u64 v[64:65], v[72:73], 0, v[48:49]
	v_lshl_add_u64 v[66:67], v[72:73], 0, v[50:51]
	v_lshl_add_u64 v[68:69], v[72:73], 0, v[52:53]
	global_load_dword v102, v[54:55], off nt
	global_load_dword v101, v[56:57], off nt
	global_load_dword v100, v[58:59], off nt
	global_load_dword v99, v[60:61], off nt
	global_load_dword v98, v[62:63], off nt
	global_load_dword v97, v[64:65], off nt
	global_load_dword v96, v[66:67], off nt
	global_load_dword v95, v[68:69], off nt
	v_lshl_add_u64 v[54:55], v[6:7], 0, s[6:7]
	s_mov_b64 s[6:7], 0xc8000
	v_lshl_add_u64 v[56:57], v[6:7], 0, s[6:7]
	s_mov_b64 s[6:7], 0xd0000
	v_lshl_add_u64 v[58:59], v[6:7], 0, s[6:7]
	s_mov_b64 s[6:7], 0xd8000
	v_lshl_add_u64 v[60:61], v[6:7], 0, s[6:7]
	s_mov_b64 s[6:7], 0xe0000
	v_lshl_add_u64 v[62:63], v[6:7], 0, s[6:7]
	s_mov_b64 s[6:7], 0xe8000
	v_lshl_add_u64 v[64:65], v[6:7], 0, s[6:7]
	s_mov_b64 s[6:7], 0xf0000
	v_lshl_add_u64 v[66:67], v[6:7], 0, s[6:7]
	s_mov_b64 s[6:7], 0xf8000
	v_lshl_add_u64 v[74:75], v[72:73], 0, v[54:55]
	v_lshl_add_u64 v[68:69], v[6:7], 0, s[6:7]
	v_lshl_add_u64 v[112:113], v[72:73], 0, v[56:57]
	v_lshl_add_u64 v[114:115], v[72:73], 0, v[58:59]
	v_lshl_add_u64 v[116:117], v[72:73], 0, v[60:61]
	v_lshl_add_u64 v[118:119], v[72:73], 0, v[62:63]
	v_lshl_add_u64 v[120:121], v[72:73], 0, v[64:65]
	v_lshl_add_u64 v[122:123], v[72:73], 0, v[66:67]
	v_lshl_add_u64 v[72:73], v[72:73], 0, v[68:69]
	global_load_dword v110, v[74:75], off nt
	global_load_dword v109, v[112:113], off nt
	global_load_dword v108, v[114:115], off nt
	global_load_dword v107, v[116:117], off nt
	global_load_dword v106, v[118:119], off nt
	global_load_dword v105, v[120:121], off nt
	global_load_dword v104, v[122:123], off nt
	global_load_dword v103, v[72:73], off nt
	v_lshl_add_u64 v[72:73], s[48:49], 0, v[70:71]
	v_add_u32_e32 v78, s3, v70
	v_and_b32_e32 v70, 48, v76
	s_movk_i32 s9, 0x84
	v_readlane_b32 s41, v254, 3
	v_readlane_b32 s42, v254, 4
	v_readlane_b32 s43, v254, 5
	s_mov_b64 s[50:51], s[54:55]
	v_mul_u32_u24_e32 v77, 0x84, v70
	v_lshl_add_u64 v[70:71], s[68:69], 0, v[70:71]
	s_mov_b64 s[6:7], 0x2000000
	v_mul_lo_u32 v111, v2, s9
	s_lshl_b32 s11, s8, 5
	v_lshl_add_u64 v[74:75], v[70:71], 0, s[6:7]
	v_add3_u32 v77, s3, v77, v5
	s_lshl_b32 s9, s10, 5
	s_mov_b32 s30, 0x8000
	s_mov_b32 s31, 0x10000
	s_mov_b32 s33, 0x18000
	s_mov_b32 s35, 0x20000
	s_mov_b32 s38, 0x28000
	s_mov_b32 s39, 0x30000
	s_mov_b32 s40, 0x38000
	s_mov_b32 s41, 0x40000
	s_mov_b32 s42, 0x48000
	s_mov_b32 s43, 0x50000
	s_mov_b32 s44, 0x58000
	s_mov_b32 s45, 0x60000
	s_mov_b32 s46, 0x68000
	s_mov_b32 s47, 0x70000
	s_mov_b32 s48, 0x78000
	s_mov_b32 s49, 0x80000
	s_mov_b32 s50, 0x88000
	s_mov_b32 s51, 0x90000
	s_mov_b32 s52, 0x98000
	s_mov_b32 s53, 0xa0000
	s_mov_b32 s54, 0xa8000
	s_mov_b32 s55, 0xb0000
	s_mov_b32 s56, 0xb8000
	s_mov_b32 s57, 0xc0000
	s_mov_b32 s58, 0xc8000
	s_mov_b32 s59, 0xd0000
	s_mov_b32 s60, 0xd8000
	v_add_u32_e32 v78, v78, v111
	s_mov_b32 s61, s11
	s_mov_b32 s64, s8
	s_branch .LBB0_2040

; template <int FP8> __device__ __forceinline__ void transpose_stream(const float* W, int K, int N, void* WT_, int split, int add, int ldt, int col_add, LAS float* scr, int it0, int its, int nitems, int lane, const float* kscale) {
;     ...
;     for (int it = it0; it < nitems; it += its) {
;         float nxt[32]; const int itn = it + its;
;         if (itn < nitems) { const int kb = itn / nblk, nb = itn % nblk;
; #pragma unroll
;             for (int i = 0; i < 32; ++i) nxt[i] = W[(size_t)(64 * kb + 2 * i + (lane >> 5)) * N + 32 * nb + (lane & 31)]; }
;         else {
; #pragma unroll
;             for (int i = 0; i < 32; ++i) nxt[i] = 0.f; }
.LBB0_2042:
	v_mov_b32_e32 v111, 0
	s_andn2_b64 vcc, exec, s[28:29]
	v_mov_b32_e32 v112, 0
	v_mov_b32_e32 v113, 0
	v_mov_b32_e32 v114, 0
	v_mov_b32_e32 v115, 0
	v_mov_b32_e32 v116, 0
	v_mov_b32_e32 v117, 0
	v_mov_b32_e32 v118, 0
	v_mov_b32_e32 v119, 0
	v_mov_b32_e32 v120, 0
	v_mov_b32_e32 v121, 0
	v_mov_b32_e32 v122, 0
	v_mov_b32_e32 v123, 0
	v_mov_b32_e32 v124, 0
	v_mov_b32_e32 v125, 0
	v_mov_b32_e32 v126, 0
	v_mov_b32_e32 v127, 0
	v_mov_b32_e32 v128, 0
	v_mov_b32_e32 v129, 0
	v_mov_b32_e32 v130, 0
	v_mov_b32_e32 v131, 0
	v_mov_b32_e32 v132, 0
	v_mov_b32_e32 v133, 0
	v_mov_b32_e32 v134, 0
	v_mov_b32_e32 v135, 0
	v_mov_b32_e32 v136, 0
	v_mov_b32_e32 v137, 0
	v_mov_b32_e32 v138, 0
	v_mov_b32_e32 v139, 0
	v_mov_b32_e32 v140, 0
	v_mov_b32_e32 v141, 0
	v_mov_b32_e32 v142, 0
	s_cbranch_vccnz .LBB0_2039
	s_ashr_i32 s28, s62, 31
	s_lshr_b32 s28, s28, 25
	s_add_i32 s28, s62, s28
	s_ashr_i32 s28, s28, 7
	v_lshl_add_u32 v112, s28, 6, v2
	s_add_i32 s63, s9, s61
	s_lshl_b32 s28, s28, 12
	s_sub_i32 s28, s63, s28
	s_ashr_i32 s29, s28, 31
	v_ashrrev_i32_e32 v113, 31, v112
	v_lshl_add_u64 v[114:115], s[28:29], 2, v[72:73]
	v_lshlrev_b64 v[112:113], 14, v[112:113]
	v_lshl_add_u64 v[136:137], v[114:115], 0, v[112:113]
	v_add_co_u32_e32 v112, vcc, s30, v136
	s_nop 1
	v_addc_co_u32_e32 v113, vcc, 0, v137, vcc
	v_add_co_u32_e32 v114, vcc, s31, v136
	s_nop 1
	v_addc_co_u32_e32 v115, vcc, 0, v137, vcc
	v_add_co_u32_e32 v116, vcc, s33, v136
	s_nop 1
	v_addc_co_u32_e32 v117, vcc, 0, v137, vcc
	v_add_co_u32_e32 v118, vcc, s35, v136
	s_nop 1
	v_addc_co_u32_e32 v119, vcc, 0, v137, vcc
	v_add_co_u32_e32 v120, vcc, s38, v136
	s_nop 1
	v_addc_co_u32_e32 v121, vcc, 0, v137, vcc
	v_add_co_u32_e32 v122, vcc, s39, v136
	s_nop 1
	v_addc_co_u32_e32 v123, vcc, 0, v137, vcc
	v_add_co_u32_e32 v124, vcc, s40, v136
	s_nop 1
	v_addc_co_u32_e32 v125, vcc, 0, v137, vcc
	global_load_dword v111, v[136:137], off nt
	s_nop 0
	global_load_dword v112, v[112:113], off nt
	s_nop 0
	global_load_dword v113, v[114:115], off nt
	s_nop 0
	global_load_dword v114, v[116:117], off nt
	global_load_dword v115, v[118:119], off nt
	s_nop 0
	global_load_dword v116, v[120:121], off nt
	global_load_dword v117, v[122:123], off nt
	global_load_dword v118, v[124:125], off nt
	v_add_co_u32_e32 v120, vcc, s41, v136
	s_nop 1
	v_addc_co_u32_e32 v121, vcc, 0, v137, vcc
	v_add_co_u32_e32 v122, vcc, s42, v136
	s_nop 1
	v_addc_co_u32_e32 v123, vcc, 0, v137, vcc
	v_add_co_u32_e32 v124, vcc, s43, v136
	s_nop 1
	v_addc_co_u32_e32 v125, vcc, 0, v137, vcc
	v_add_co_u32_e32 v126, vcc, s44, v136
	s_nop 1
	v_addc_co_u32_e32 v127, vcc, 0, v137, vcc
	v_add_co_u32_e32 v128, vcc, s45, v136
	s_nop 1
	v_addc_co_u32_e32 v129, vcc, 0, v137, vcc
	v_add_co_u32_e32 v130, vcc, s46, v136
	s_nop 1
	v_addc_co_u32_e32 v131, vcc, 0, v137, vcc
	v_add_co_u32_e32 v132, vcc, s47, v136
	s_nop 1
	v_addc_co_u32_e32 v133, vcc, 0, v137, vcc
	v_add_co_u32_e32 v134, vcc, s48, v136
	s_nop 1
	v_addc_co_u32_e32 v135, vcc, 0, v137, vcc
	global_load_dword v119, v[120:121], off nt
	s_nop 0
	global_load_dword v120, v[122:123], off nt
	global_load_dword v121, v[124:125], off nt
	s_nop 0
	global_load_dword v122, v[126:127], off nt
	global_load_dword v123, v[128:129], off nt
	global_load_dword v124, v[130:131], off nt
	global_load_dword v125, v[132:133], off nt
	s_nop 0
	global_load_dword v126, v[134:135], off nt
	v_add_co_u32_e32 v128, vcc, s49, v136
	s_nop 1
	v_addc_co_u32_e32 v129, vcc, 0, v137, vcc
	v_add_co_u32_e32 v130, vcc, s50, v136
	s_nop 1
	v_addc_co_u32_e32 v131, vcc, 0, v137, vcc
	v_add_co_u32_e32 v132, vcc, s51, v136
	s_nop 1
	v_addc_co_u32_e32 v133, vcc, 0, v137, vcc
	v_add_co_u32_e32 v134, vcc, s52, v136
	s_nop 1
	v_addc_co_u32_e32 v135, vcc, 0, v137, vcc
	v_add_co_u32_e32 v138, vcc, s53, v136
	s_nop 1
	v_addc_co_u32_e32 v139, vcc, 0, v137, vcc
	v_add_co_u32_e32 v140, vcc, s54, v136
	s_nop 1
	v_addc_co_u32_e32 v141, vcc, 0, v137, vcc
	v_add_co_u32_e32 v142, vcc, s55, v136
	s_nop 1
	v_addc_co_u32_e32 v143, vcc, 0, v137, vcc
	v_add_co_u32_e32 v144, vcc, s56, v136
	s_nop 1
	v_addc_co_u32_e32 v145, vcc, 0, v137, vcc
	global_load_dword v127, v[128:129], off nt
	s_nop 0
	global_load_dword v128, v[130:131], off nt
	global_load_dword v129, v[132:133], off nt
	s_nop 0
	global_load_dword v130, v[134:135], off nt
	global_load_dword v131, v[138:139], off nt
	global_load_dword v132, v[140:141], off nt
	global_load_dword v133, v[142:143], off nt
	s_nop 0
	global_load_dword v134, v[144:145], off nt
	v_add_co_u32_e32 v138, vcc, s57, v136
	s_nop 1
	v_addc_co_u32_e32 v139, vcc, 0, v137, vcc
	v_add_co_u32_e32 v140, vcc, s58, v136
	s_nop 1
	v_addc_co_u32_e32 v141, vcc, 0, v137, vcc
	v_add_co_u32_e32 v142, vcc, s59, v136
	s_nop 1
	v_addc_co_u32_e32 v143, vcc, 0, v137, vcc
	v_add_co_u32_e32 v144, vcc, s60, v136
	s_nop 1
	v_addc_co_u32_e32 v145, vcc, 0, v137, vcc
	v_add_co_u32_e32 v150, vcc, 0xe0000, v136
	s_nop 1
	v_addc_co_u32_e32 v151, vcc, 0, v137, vcc
	v_add_co_u32_e32 v152, vcc, 0xe8000, v136
	s_nop 1
	v_addc_co_u32_e32 v153, vcc, 0, v137, vcc
	v_add_co_u32_e32 v154, vcc, 0xf0000, v136
	s_nop 1
	v_addc_co_u32_e32 v155, vcc, 0, v137, vcc
	v_add_co_u32_e32 v156, vcc, 0xf8000, v136
	s_nop 1
	v_addc_co_u32_e32 v157, vcc, 0, v137, vcc
	global_load_dword v135, v[138:139], off nt
	global_load_dword v136, v[140:141], off nt
	global_load_dword v137, v[142:143], off nt
	s_nop 0
	global_load_dword v138, v[144:145], off nt
	global_load_dword v139, v[150:151], off nt
	global_load_dword v140, v[152:153], off nt
	global_load_dword v141, v[154:155], off nt
	global_load_dword v142, v[156:157], off nt
	s_branch .LBB0_2039
; template <int FP8> __device__ __forceinline__ void transpose_stream(const float* W, int K, int N, void* WT_, int split, int add, int ldt, int col_add, LAS float* scr, int it0, int its, int nitems, int lane, const float* kscale) {
;     const int nblk = N / 32; float cur[32];
;     if (it0 < nitems) { const int kb = it0 / nblk, nb = it0 % nblk;
; #pragma unroll
;         for (int i = 0; i < 32; ++i) cur[i] = W[(size_t)(64 * kb + 2 * i + (lane >> 5)) * N + 32 * nb + (lane & 31)]; }
; __device__ __forceinline__ void late_prep(Frame& F, int mgw, int mngw) {
;     ...
;     transpose_stream<true>(F.in[15], RW, D_, F.ws + WS_WPA, 1 << 30, 0, 4096, 2048, scr, mgw, mngw, I_PA, F.lane, nullptr);
.LBB0_2044:
	v_readlane_b32 s40, v254, 2
	v_readlane_b32 s50, v254, 12
	v_readlane_b32 s51, v254, 13
	v_readlane_b32 s54, v254, 16
	v_readlane_b32 s55, v254, 17
	s_mov_b64 s[50:51], s[54:55]
	s_add_u32 s0, s50, s0
	s_addc_u32 s1, s51, s1
	v_lshlrev_b32_e32 v72, 2, v4
	v_mov_b32_e32 v73, 0
	v_lshl_add_u64 v[74:75], s[0:1], 0, v[72:73]
	v_lshl_add_u64 v[6:7], v[74:75], 0, v[6:7]
	v_lshl_add_u64 v[8:9], v[74:75], 0, v[8:9]
	v_lshl_add_u64 v[80:81], v[74:75], 0, v[10:11]
	v_lshl_add_u64 v[82:83], v[74:75], 0, v[12:13]
	v_lshl_add_u64 v[84:85], v[74:75], 0, v[14:15]
	v_lshl_add_u64 v[86:87], v[74:75], 0, v[16:17]
	v_lshl_add_u64 v[18:19], v[74:75], 0, v[18:19]
	v_lshl_add_u64 v[20:21], v[74:75], 0, v[20:21]
	global_load_dword v17, v[6:7], off nt
	global_load_dword v16, v[8:9], off nt
	global_load_dword v15, v[80:81], off nt
	global_load_dword v14, v[82:83], off nt
	global_load_dword v13, v[84:85], off nt
	global_load_dword v12, v[86:87], off nt
	global_load_dword v11, v[18:19], off nt
	global_load_dword v10, v[20:21], off nt
	v_lshl_add_u64 v[6:7], v[74:75], 0, v[22:23]
	v_lshl_add_u64 v[8:9], v[74:75], 0, v[24:25]
	v_lshl_add_u64 v[26:27], v[74:75], 0, v[26:27]
	v_lshl_add_u64 v[28:29], v[74:75], 0, v[28:29]
	v_lshl_add_u64 v[30:31], v[74:75], 0, v[30:31]
	v_lshl_add_u64 v[32:33], v[74:75], 0, v[32:33]
	v_lshl_add_u64 v[34:35], v[74:75], 0, v[34:35]
	v_lshl_add_u64 v[36:37], v[74:75], 0, v[36:37]
	global_load_dword v25, v[6:7], off nt
	global_load_dword v24, v[8:9], off nt
	global_load_dword v23, v[26:27], off nt
	global_load_dword v22, v[28:29], off nt
	global_load_dword v21, v[30:31], off nt
	global_load_dword v20, v[32:33], off nt
	global_load_dword v19, v[34:35], off nt
	global_load_dword v18, v[36:37], off nt
	v_lshl_add_u64 v[6:7], v[74:75], 0, v[38:39]
	v_lshl_add_u64 v[8:9], v[74:75], 0, v[40:41]
	v_lshl_add_u64 v[34:35], v[74:75], 0, v[42:43]
	v_lshl_add_u64 v[36:37], v[74:75], 0, v[44:45]
	v_lshl_add_u64 v[38:39], v[74:75], 0, v[46:47]
	v_lshl_add_u64 v[40:41], v[74:75], 0, v[48:49]
	v_lshl_add_u64 v[42:43], v[74:75], 0, v[50:51]
	v_lshl_add_u64 v[44:45], v[74:75], 0, v[52:53]
	global_load_dword v33, v[6:7], off nt
	global_load_dword v32, v[8:9], off nt
	global_load_dword v31, v[34:35], off nt
	global_load_dword v30, v[36:37], off nt
	global_load_dword v29, v[38:39], off nt
	global_load_dword v28, v[40:41], off nt
	global_load_dword v27, v[42:43], off nt
	global_load_dword v26, v[44:45], off nt
	v_lshl_add_u64 v[6:7], v[74:75], 0, v[54:55]
	v_lshl_add_u64 v[8:9], v[74:75], 0, v[56:57]
	v_lshl_add_u64 v[42:43], v[74:75], 0, v[58:59]
	v_lshl_add_u64 v[44:45], v[74:75], 0, v[60:61]
	v_lshl_add_u64 v[46:47], v[74:75], 0, v[62:63]
	v_lshl_add_u64 v[48:49], v[74:75], 0, v[64:65]
	v_lshl_add_u64 v[50:51], v[74:75], 0, v[66:67]
	v_lshl_add_u64 v[52:53], v[74:75], 0, v[68:69]
	global_load_dword v41, v[6:7], off nt
	global_load_dword v40, v[8:9], off nt
	global_load_dword v39, v[42:43], off nt
	global_load_dword v38, v[44:45], off nt
	global_load_dword v37, v[46:47], off nt
	global_load_dword v36, v[48:49], off nt
	global_load_dword v35, v[50:51], off nt
	global_load_dword v34, v[52:53], off nt
	v_readlane_b32 s41, v254, 3
	v_readlane_b32 s42, v254, 4
	v_readlane_b32 s43, v254, 5
	v_readlane_b32 s44, v254, 6
	v_readlane_b32 s45, v254, 7
	v_readlane_b32 s46, v254, 8
	v_readlane_b32 s47, v254, 9
	v_readlane_b32 s48, v254, 10
	v_readlane_b32 s49, v254, 11
	v_readlane_b32 s52, v254, 14
	v_readlane_b32 s53, v254, 15
	s_mov_b64 s[0:1], 0x2000800
	v_lshl_add_u64 v[6:7], s[50:51], 0, v[72:73]
	v_lshl_add_u64 v[8:9], v[70:71], 0, s[0:1]
	s_mov_b32 s28, 0x8000
	s_mov_b32 s29, 0x10000
	s_mov_b32 s30, 0x18000
	s_mov_b32 s31, 0x20000
	s_mov_b32 s33, 0x28000
	s_mov_b32 s35, 0x30000
	s_mov_b32 s38, 0x38000
	s_mov_b32 s39, 0x40000
	s_mov_b32 s40, 0x48000
	s_mov_b32 s41, 0x50000
	s_mov_b32 s42, 0x58000
	s_mov_b32 s43, 0x60000
	s_mov_b32 s44, 0x68000
	s_mov_b32 s45, 0x70000
	s_mov_b32 s46, 0x78000
	s_mov_b32 s47, 0x80000
	s_mov_b32 s48, 0x88000
	s_mov_b32 s49, 0x90000
	s_mov_b32 s50, 0x98000
	s_mov_b32 s51, 0xa0000
	s_mov_b32 s52, 0xa8000
	s_mov_b32 s53, 0xb0000
	s_mov_b32 s54, 0xb8000
	s_mov_b32 s55, 0xc0000
	s_mov_b32 s56, 0xc8000
	s_mov_b32 s57, 0xd0000
	s_mov_b32 s58, 0xd8000
	s_mov_b32 s61, s8
	s_branch .LBB0_2046

; template <int FP8> __device__ __forceinline__ void transpose_stream(const float* W, int K, int N, void* WT_, int split, int add, int ldt, int col_add, LAS float* scr, int it0, int its, int nitems, int lane, const float* kscale) {
;     ...
;     for (int it = it0; it < nitems; it += its) {
;         float nxt[32]; const int itn = it + its;
;         if (itn < nitems) { const int kb = itn / nblk, nb = itn % nblk;
; #pragma unroll
;             for (int i = 0; i < 32; ++i) nxt[i] = W[(size_t)(64 * kb + 2 * i + (lane >> 5)) * N + 32 * nb + (lane & 31)]; }
;         else {
; #pragma unroll
;             for (int i = 0; i < 32; ++i) nxt[i] = 0.f; }
.LBB0_2048:
	v_mov_b32_e32 v42, 0
	s_andn2_b64 vcc, exec, s[6:7]
	v_mov_b32_e32 v43, 0
	v_mov_b32_e32 v44, 0
	v_mov_b32_e32 v45, 0
	v_mov_b32_e32 v46, 0
	v_mov_b32_e32 v47, 0
	v_mov_b32_e32 v48, 0
	v_mov_b32_e32 v49, 0
	v_mov_b32_e32 v50, 0
	v_mov_b32_e32 v51, 0
	v_mov_b32_e32 v52, 0
	v_mov_b32_e32 v53, 0
	v_mov_b32_e32 v54, 0
	v_mov_b32_e32 v55, 0
	v_mov_b32_e32 v56, 0
	v_mov_b32_e32 v57, 0
	v_mov_b32_e32 v58, 0
	v_mov_b32_e32 v59, 0
	v_mov_b32_e32 v60, 0
	v_mov_b32_e32 v61, 0
	v_mov_b32_e32 v62, 0
	v_mov_b32_e32 v63, 0
	v_mov_b32_e32 v64, 0
	v_mov_b32_e32 v65, 0
	v_mov_b32_e32 v66, 0
	v_mov_b32_e32 v67, 0
	v_mov_b32_e32 v68, 0
	v_mov_b32_e32 v69, 0
	v_mov_b32_e32 v70, 0
	v_mov_b32_e32 v71, 0
	v_mov_b32_e32 v72, 0
	v_mov_b32_e32 v73, 0
	s_cbranch_vccnz .LBB0_2045
	s_ashr_i32 s6, s59, 31
	s_lshr_b32 s6, s6, 25
	s_add_i32 s6, s59, s6
	s_ashr_i32 s6, s6, 7
	v_lshl_add_u32 v42, s6, 6, v2
	s_add_i32 s60, s9, s11
	s_lshl_b32 s6, s6, 12
	s_sub_i32 s6, s60, s6
	s_ashr_i32 s7, s6, 31
	v_ashrrev_i32_e32 v43, 31, v42
	v_lshl_add_u64 v[44:45], s[6:7], 2, v[6:7]
	v_lshlrev_b64 v[42:43], 14, v[42:43]
	v_lshl_add_u64 v[66:67], v[44:45], 0, v[42:43]
	v_add_co_u32_e32 v44, vcc, s28, v66
	s_nop 1
	v_addc_co_u32_e32 v45, vcc, 0, v67, vcc
	v_add_co_u32_e32 v46, vcc, s29, v66
	s_nop 1
	v_addc_co_u32_e32 v47, vcc, 0, v67, vcc
	v_add_co_u32_e32 v48, vcc, s30, v66
	s_nop 1
	v_addc_co_u32_e32 v49, vcc, 0, v67, vcc
	v_add_co_u32_e32 v50, vcc, s31, v66
	s_nop 1
	v_addc_co_u32_e32 v51, vcc, 0, v67, vcc
	v_add_co_u32_e32 v52, vcc, s33, v66
	s_nop 1
	v_addc_co_u32_e32 v53, vcc, 0, v67, vcc
	v_add_co_u32_e32 v54, vcc, s35, v66
	s_nop 1
	v_addc_co_u32_e32 v55, vcc, 0, v67, vcc
	v_add_co_u32_e32 v56, vcc, s38, v66
	s_nop 1
	v_addc_co_u32_e32 v57, vcc, 0, v67, vcc
	global_load_dword v42, v[66:67], off nt
	global_load_dword v43, v[44:45], off nt
	s_nop 0
	global_load_dword v44, v[46:47], off nt
	global_load_dword v45, v[48:49], off nt
	s_nop 0
	global_load_dword v46, v[50:51], off nt
	global_load_dword v47, v[52:53], off nt
	global_load_dword v48, v[54:55], off nt
	global_load_dword v49, v[56:57], off nt
	v_add_co_u32_e32 v50, vcc, s39, v66
	s_nop 1
	v_addc_co_u32_e32 v51, vcc, 0, v67, vcc
	v_add_co_u32_e32 v52, vcc, s40, v66
	s_nop 1
	v_addc_co_u32_e32 v53, vcc, 0, v67, vcc
	v_add_co_u32_e32 v54, vcc, s41, v66
	s_nop 1
	v_addc_co_u32_e32 v55, vcc, 0, v67, vcc
	v_add_co_u32_e32 v56, vcc, s42, v66
	s_nop 1
	v_addc_co_u32_e32 v57, vcc, 0, v67, vcc
	v_add_co_u32_e32 v58, vcc, s43, v66
	s_nop 1
	v_addc_co_u32_e32 v59, vcc, 0, v67, vcc
	v_add_co_u32_e32 v60, vcc, s44, v66
	s_nop 1
	v_addc_co_u32_e32 v61, vcc, 0, v67, vcc
	v_add_co_u32_e32 v62, vcc, s45, v66
	s_nop 1
	v_addc_co_u32_e32 v63, vcc, 0, v67, vcc
	v_add_co_u32_e32 v64, vcc, s46, v66
	s_nop 1
	v_addc_co_u32_e32 v65, vcc, 0, v67, vcc
	global_load_dword v50, v[50:51], off nt
	s_nop 0
	global_load_dword v51, v[52:53], off nt
	s_nop 0
	global_load_dword v52, v[54:55], off nt
	global_load_dword v53, v[56:57], off nt
	s_nop 0
	global_load_dword v54, v[58:59], off nt
	global_load_dword v55, v[60:61], off nt
	global_load_dword v56, v[62:63], off nt
	global_load_dword v57, v[64:65], off nt
	v_add_co_u32_e32 v58, vcc, s47, v66
	s_nop 1
	v_addc_co_u32_e32 v59, vcc, 0, v67, vcc
	v_add_co_u32_e32 v60, vcc, s48, v66
	s_nop 1
	v_addc_co_u32_e32 v61, vcc, 0, v67, vcc
	v_add_co_u32_e32 v62, vcc, s49, v66
	s_nop 1
	v_addc_co_u32_e32 v63, vcc, 0, v67, vcc
	v_add_co_u32_e32 v64, vcc, s50, v66
	s_nop 1
	v_addc_co_u32_e32 v65, vcc, 0, v67, vcc
	v_add_co_u32_e32 v68, vcc, s51, v66
	s_nop 1
	v_addc_co_u32_e32 v69, vcc, 0, v67, vcc
	v_add_co_u32_e32 v70, vcc, s52, v66
	s_nop 1
	v_addc_co_u32_e32 v71, vcc, 0, v67, vcc
	v_add_co_u32_e32 v72, vcc, s53, v66
	s_nop 1
	v_addc_co_u32_e32 v73, vcc, 0, v67, vcc
	v_add_co_u32_e32 v74, vcc, s54, v66
	s_nop 1
	v_addc_co_u32_e32 v75, vcc, 0, v67, vcc
	global_load_dword v58, v[58:59], off nt
	s_nop 0
	global_load_dword v59, v[60:61], off nt
	s_nop 0
	global_load_dword v60, v[62:63], off nt
	global_load_dword v61, v[64:65], off nt
	s_nop 0
	global_load_dword v62, v[68:69], off nt
	global_load_dword v63, v[70:71], off nt
	global_load_dword v64, v[72:73], off nt
	global_load_dword v65, v[74:75], off nt
	v_add_co_u32_e32 v68, vcc, s55, v66
	s_nop 1
	v_addc_co_u32_e32 v69, vcc, 0, v67, vcc
	v_add_co_u32_e32 v70, vcc, s56, v66
	s_nop 1
	v_addc_co_u32_e32 v71, vcc, 0, v67, vcc
	v_add_co_u32_e32 v72, vcc, s57, v66
	s_nop 1
	v_addc_co_u32_e32 v73, vcc, 0, v67, vcc
	v_add_co_u32_e32 v74, vcc, s58, v66
	s_nop 1
	v_addc_co_u32_e32 v75, vcc, 0, v67, vcc
	v_add_co_u32_e32 v80, vcc, 0xe0000, v66
	s_nop 1
	v_addc_co_u32_e32 v81, vcc, 0, v67, vcc
	v_add_co_u32_e32 v82, vcc, 0xe8000, v66
	s_nop 1
	v_addc_co_u32_e32 v83, vcc, 0, v67, vcc
	v_add_co_u32_e32 v84, vcc, 0xf0000, v66
	s_nop 1
	v_addc_co_u32_e32 v85, vcc, 0, v67, vcc
	v_add_co_u32_e32 v86, vcc, 0xf8000, v66
	s_nop 1
	v_addc_co_u32_e32 v87, vcc, 0, v67, vcc
	global_load_dword v66, v[68:69], off nt
	global_load_dword v67, v[70:71], off nt
	s_nop 0
	global_load_dword v68, v[72:73], off nt
	global_load_dword v69, v[74:75], off nt
	global_load_dword v70, v[80:81], off nt
	global_load_dword v71, v[82:83], off nt
	s_nop 0
	global_load_dword v72, v[84:85], off nt
	global_load_dword v73, v[86:87], off nt
	s_branch .LBB0_2045
; template <int FP8> __device__ __forceinline__ void transpose_stream(const float* W, int K, int N, void* WT_, int split, int add, int ldt, int col_add, LAS float* scr, int it0, int its, int nitems, int lane, const float* kscale) {
;     const int nblk = N / 32; float cur[32];
;     if (it0 < nitems) { const int kb = it0 / nblk, nb = it0 % nblk;
; #pragma unroll
;         for (int i = 0; i < 32; ++i) cur[i] = W[(size_t)(64 * kb + 2 * i + (lane >> 5)) * N + 32 * nb + (lane & 31)]; }
; __device__ __forceinline__ void late_prep(Frame& F, int mgw, int mngw) {
;     ...
;     transpose_stream<true>(F.in[16], D_, D_, F.ws + WS_WOUT, 1 << 30, 0, 0, 0, scr, mgw, mngw, I_OUT, F.lane, nullptr);
.LBB0_2050:
	s_cmpk_gt_i32 s8, 0x1fff
	s_cbranch_scc1 .LBB0_2057
	s_ashr_i32 s0, s8, 31
	s_lshr_b32 s0, s0, 25
	s_add_i32 s0, s8, s0
	s_ashr_i32 s1, s0, 7
	s_and_b32 s0, s0, 0x7ffff80
	s_sub_i32 s0, s8, s0
	s_lshl_b32 s0, s0, 5
	s_waitcnt vmcnt(10)
	v_lshl_add_u32 v6, s1, 6, v2
	s_ashr_i32 s1, s0, 31
	s_lshl_b64 s[0:1], s[0:1], 2
	s_add_u32 s0, s12, s0
	v_lshlrev_b32_e32 v7, 2, v148
	s_addc_u32 s1, s13, s1
	v_and_b32_e32 v8, 0x7c, v7
	v_mov_b32_e32 v9, 0
	v_ashrrev_i32_e32 v7, 31, v6
	s_waitcnt vmcnt(9)
	v_lshl_add_u64 v[10:11], s[0:1], 0, v[8:9]
	v_lshlrev_b64 v[6:7], 14, v[6:7]
	v_lshl_add_u64 v[6:7], v[10:11], 0, v[6:7]
	s_mov_b32 s9, 0x8000
	v_add_co_u32_e32 v10, vcc, s9, v6
	s_mov_b32 s11, 0x10000
	s_nop 0
	v_addc_co_u32_e32 v11, vcc, 0, v7, vcc
	v_add_co_u32_e32 v12, vcc, s11, v6
	s_mov_b32 s28, 0x18000
	s_nop 0
	v_addc_co_u32_e32 v13, vcc, 0, v7, vcc
	s_waitcnt vmcnt(8)
	v_add_co_u32_e32 v14, vcc, s28, v6
	s_mov_b32 s29, 0x20000
	s_nop 0
	v_addc_co_u32_e32 v15, vcc, 0, v7, vcc
	s_waitcnt vmcnt(7)
	v_add_co_u32_e32 v20, vcc, s29, v6
	s_mov_b32 s30, 0x28000
	s_nop 0
	v_addc_co_u32_e32 v21, vcc, 0, v7, vcc
	s_waitcnt vmcnt(6)
	v_add_co_u32_e32 v22, vcc, s30, v6
	s_mov_b32 s31, 0x30000
	s_nop 0
	v_addc_co_u32_e32 v23, vcc, 0, v7, vcc
	v_add_co_u32_e32 v24, vcc, s31, v6
	s_mov_b32 s33, 0x38000
	s_nop 0
	v_addc_co_u32_e32 v25, vcc, 0, v7, vcc
	s_waitcnt vmcnt(5)
	v_add_co_u32_e32 v26, vcc, s33, v6
	s_mov_b32 s35, 0x40000
	s_nop 0
	v_addc_co_u32_e32 v27, vcc, 0, v7, vcc
	global_load_dword v18, v[6:7], off nt
	global_load_dword v17, v[10:11], off nt
	global_load_dword v16, v[12:13], off nt
	s_nop 0
	global_load_dword v15, v[14:15], off nt
	s_nop 0
	global_load_dword v13, v[20:21], off nt
	global_load_dword v12, v[22:23], off nt
	global_load_dword v11, v[24:25], off nt
	global_load_dword v14, v[26:27], off nt
	v_add_co_u32_e32 v20, vcc, s35, v6
	s_mov_b32 s38, 0x48000
	s_nop 0
	v_addc_co_u32_e32 v21, vcc, 0, v7, vcc
	v_add_co_u32_e32 v22, vcc, s38, v6
	s_mov_b32 s39, 0x50000
	s_nop 0
	v_addc_co_u32_e32 v23, vcc, 0, v7, vcc
	v_add_co_u32_e32 v28, vcc, s39, v6
	s_mov_b32 s40, 0x58000
	s_nop 0
	v_addc_co_u32_e32 v29, vcc, 0, v7, vcc
	s_waitcnt vmcnt(12)
	v_add_co_u32_e32 v30, vcc, s40, v6
	s_mov_b32 s41, 0x60000
	s_nop 0
	v_addc_co_u32_e32 v31, vcc, 0, v7, vcc
	v_add_co_u32_e32 v32, vcc, s41, v6
	s_mov_b32 s42, 0x68000
	s_nop 0
	v_addc_co_u32_e32 v33, vcc, 0, v7, vcc
	s_waitcnt vmcnt(11)
	v_add_co_u32_e32 v34, vcc, s42, v6
	s_mov_b32 s43, 0x70000
	s_nop 0
	v_addc_co_u32_e32 v35, vcc, 0, v7, vcc
	v_add_co_u32_e32 v36, vcc, s43, v6
	s_mov_b32 s44, 0x78000
	s_nop 0
	v_addc_co_u32_e32 v37, vcc, 0, v7, vcc
	s_waitcnt vmcnt(10)
	v_add_co_u32_e32 v38, vcc, s44, v6
	s_mov_b32 s45, 0x80000
	s_nop 0
	v_addc_co_u32_e32 v39, vcc, 0, v7, vcc
	global_load_dword v26, v[20:21], off nt
	global_load_dword v25, v[22:23], off nt
	global_load_dword v24, v[28:29], off nt
	s_nop 0
	global_load_dword v23, v[30:31], off nt
	global_load_dword v21, v[32:33], off nt
	global_load_dword v20, v[34:35], off nt
	global_load_dword v19, v[36:37], off nt
	global_load_dword v22, v[38:39], off nt
	v_add_co_u32_e32 v28, vcc, s45, v6
	s_mov_b32 s46, 0x88000
	s_nop 0
	v_addc_co_u32_e32 v29, vcc, 0, v7, vcc
	v_add_co_u32_e32 v30, vcc, s46, v6
	s_mov_b32 s47, 0x90000
	s_nop 0
	v_addc_co_u32_e32 v31, vcc, 0, v7, vcc
	v_add_co_u32_e32 v36, vcc, s47, v6
	s_mov_b32 s48, 0x98000
	s_nop 0
	v_addc_co_u32_e32 v37, vcc, 0, v7, vcc
	v_add_co_u32_e32 v38, vcc, s48, v6
	s_mov_b32 s49, 0xa0000
	s_nop 0
	v_addc_co_u32_e32 v39, vcc, 0, v7, vcc
	v_add_co_u32_e32 v40, vcc, s49, v6
	s_mov_b32 s50, 0xa8000
	s_nop 0
	v_addc_co_u32_e32 v41, vcc, 0, v7, vcc
	s_waitcnt vmcnt(17)
	v_add_co_u32_e32 v42, vcc, s50, v6
	s_mov_b32 s51, 0xb0000
	s_nop 0
	v_addc_co_u32_e32 v43, vcc, 0, v7, vcc
	v_add_co_u32_e32 v44, vcc, s51, v6
	s_mov_b32 s52, 0xb8000
	s_nop 0
	v_addc_co_u32_e32 v45, vcc, 0, v7, vcc
	s_waitcnt vmcnt(16)
	v_add_co_u32_e32 v46, vcc, s52, v6
	s_mov_b32 s53, 0xc0000
	s_nop 0
	v_addc_co_u32_e32 v47, vcc, 0, v7, vcc
	global_load_dword v34, v[28:29], off nt
	global_load_dword v33, v[30:31], off nt
	global_load_dword v32, v[36:37], off nt
	s_nop 0
	global_load_dword v31, v[38:39], off nt
	global_load_dword v29, v[40:41], off nt
	global_load_dword v28, v[42:43], off nt
	global_load_dword v27, v[44:45], off nt
	global_load_dword v30, v[46:47], off nt
	v_add_co_u32_e32 v36, vcc, s53, v6
	s_mov_b32 s54, 0xc8000
	s_nop 0
	v_addc_co_u32_e32 v37, vcc, 0, v7, vcc
	v_add_co_u32_e32 v38, vcc, s54, v6
	s_mov_b32 s55, 0xd0000
	s_nop 0
	v_addc_co_u32_e32 v39, vcc, 0, v7, vcc
	v_add_co_u32_e32 v44, vcc, s55, v6
	s_mov_b32 s56, 0xd8000
	s_nop 0
	v_addc_co_u32_e32 v45, vcc, 0, v7, vcc
	v_add_co_u32_e32 v46, vcc, s56, v6
	s_mov_b32 s0, 0xe0000
	s_nop 0
	v_addc_co_u32_e32 v47, vcc, 0, v7, vcc
	v_add_co_u32_e32 v48, vcc, s0, v6
	s_mov_b32 s0, 0xe8000
	s_nop 0
	v_addc_co_u32_e32 v49, vcc, 0, v7, vcc
	v_add_co_u32_e32 v50, vcc, s0, v6
	s_mov_b32 s0, 0xf0000
	s_nop 0
	v_addc_co_u32_e32 v51, vcc, 0, v7, vcc
	v_add_co_u32_e32 v52, vcc, s0, v6
	s_mov_b32 s0, 0xf8000
	s_nop 0
	v_addc_co_u32_e32 v53, vcc, 0, v7, vcc
	v_add_co_u32_e32 v6, vcc, s0, v6
	v_add_u32_e32 v10, s3, v8
	s_nop 0
	v_addc_co_u32_e32 v7, vcc, 0, v7, vcc
	global_load_dword v42, v[36:37], off nt
	global_load_dword v41, v[38:39], off nt
	global_load_dword v40, v[44:45], off nt
	s_nop 0
	global_load_dword v39, v[46:47], off nt
	global_load_dword v37, v[48:49], off nt
	global_load_dword v36, v[50:51], off nt
	global_load_dword v35, v[52:53], off nt
	global_load_dword v38, v[6:7], off nt
	v_lshl_add_u64 v[6:7], s[12:13], 0, v[8:9]
	v_and_b32_e32 v8, 48, v76
	s_movk_i32 s6, 0x84
	v_mul_u32_u24_e32 v43, 0x84, v8
	v_lshl_add_u64 v[8:9], s[68:69], 0, v[8:9]
	s_mov_b64 s[0:1], 0x4000000
	v_mul_lo_u32 v44, v2, s6
	v_lshl_add_u64 v[8:9], v[8:9], 0, s[0:1]
	v_add3_u32 v5, s3, v43, v5
	s_lshl_b32 s13, s8, 5
	s_lshl_b32 s12, s10, 5
	v_add_u32_e32 v10, v10, v44
	s_mov_b32 s59, s8
	s_branch .LBB0_2053

; template <int FP8> __device__ __forceinline__ void transpose_stream(const float* W, int K, int N, void* WT_, int split, int add, int ldt, int col_add, LAS float* scr, int it0, int its, int nitems, int lane, const float* kscale) {
;     ...
;     for (int it = it0; it < nitems; it += its) {
;         float nxt[32]; const int itn = it + its;
;         if (itn < nitems) { const int kb = itn / nblk, nb = itn % nblk;
; #pragma unroll
;             for (int i = 0; i < 32; ++i) nxt[i] = W[(size_t)(64 * kb + 2 * i + (lane >> 5)) * N + 32 * nb + (lane & 31)]; }
;         else {
; #pragma unroll
;             for (int i = 0; i < 32; ++i) nxt[i] = 0.f; }
.LBB0_2055:
	v_mov_b32_e32 v43, 0
	s_andn2_b64 vcc, exec, s[6:7]
	v_mov_b32_e32 v44, 0
	v_mov_b32_e32 v45, 0
	v_mov_b32_e32 v46, 0
	v_mov_b32_e32 v47, 0
	v_mov_b32_e32 v48, 0
	v_mov_b32_e32 v49, 0
	v_mov_b32_e32 v50, 0
	v_mov_b32_e32 v51, 0
	v_mov_b32_e32 v52, 0
	v_mov_b32_e32 v53, 0
	v_mov_b32_e32 v54, 0
	v_mov_b32_e32 v55, 0
	v_mov_b32_e32 v56, 0
	v_mov_b32_e32 v57, 0
	v_mov_b32_e32 v58, 0
	v_mov_b32_e32 v59, 0
	v_mov_b32_e32 v60, 0
	v_mov_b32_e32 v61, 0
	v_mov_b32_e32 v62, 0
	v_mov_b32_e32 v63, 0
	v_mov_b32_e32 v64, 0
	v_mov_b32_e32 v65, 0
	v_mov_b32_e32 v66, 0
	v_mov_b32_e32 v67, 0
	v_mov_b32_e32 v68, 0
	v_mov_b32_e32 v69, 0
	v_mov_b32_e32 v70, 0
	v_mov_b32_e32 v71, 0
	v_mov_b32_e32 v72, 0
	v_mov_b32_e32 v73, 0
	v_mov_b32_e32 v74, 0
	s_cbranch_vccnz .LBB0_2052
	s_ashr_i32 s6, s57, 31
	s_lshr_b32 s6, s6, 25
	s_add_i32 s6, s57, s6
	s_ashr_i32 s6, s6, 7
	v_lshl_add_u32 v44, s6, 6, v2
	s_add_i32 s58, s12, s13
	s_lshl_b32 s6, s6, 12
	s_sub_i32 s6, s58, s6
	s_ashr_i32 s7, s6, 31
	v_ashrrev_i32_e32 v45, 31, v44
	v_lshl_add_u64 v[46:47], s[6:7], 2, v[6:7]
	v_lshlrev_b64 v[44:45], 14, v[44:45]
	v_lshl_add_u64 v[68:69], v[46:47], 0, v[44:45]
	v_add_co_u32_e32 v44, vcc, s9, v68
	s_nop 1
	v_addc_co_u32_e32 v45, vcc, 0, v69, vcc
	v_add_co_u32_e32 v46, vcc, s11, v68
	s_nop 1
	v_addc_co_u32_e32 v47, vcc, 0, v69, vcc
	v_add_co_u32_e32 v48, vcc, s28, v68
	s_nop 1
	v_addc_co_u32_e32 v49, vcc, 0, v69, vcc
	v_add_co_u32_e32 v50, vcc, s29, v68
	s_nop 1
	v_addc_co_u32_e32 v51, vcc, 0, v69, vcc
	v_add_co_u32_e32 v52, vcc, s30, v68
	s_nop 1
	v_addc_co_u32_e32 v53, vcc, 0, v69, vcc
	v_add_co_u32_e32 v54, vcc, s31, v68
	s_nop 1
	v_addc_co_u32_e32 v55, vcc, 0, v69, vcc
	v_add_co_u32_e32 v56, vcc, s33, v68
	s_nop 1
	v_addc_co_u32_e32 v57, vcc, 0, v69, vcc
	global_load_dword v43, v[68:69], off nt
	s_nop 0
	global_load_dword v44, v[44:45], off nt
	s_nop 0
	global_load_dword v45, v[46:47], off nt
	s_nop 0
	global_load_dword v46, v[48:49], off nt
	global_load_dword v47, v[50:51], off nt
	s_nop 0
	global_load_dword v48, v[52:53], off nt
	global_load_dword v49, v[54:55], off nt
	global_load_dword v50, v[56:57], off nt
	v_add_co_u32_e32 v52, vcc, s35, v68
	s_nop 1
	v_addc_co_u32_e32 v53, vcc, 0, v69, vcc
	v_add_co_u32_e32 v54, vcc, s38, v68
	s_nop 1
	v_addc_co_u32_e32 v55, vcc, 0, v69, vcc
	v_add_co_u32_e32 v56, vcc, s39, v68
	s_nop 1
	v_addc_co_u32_e32 v57, vcc, 0, v69, vcc
	v_add_co_u32_e32 v58, vcc, s40, v68
	s_nop 1
	v_addc_co_u32_e32 v59, vcc, 0, v69, vcc
	v_add_co_u32_e32 v60, vcc, s41, v68
	s_nop 1
	v_addc_co_u32_e32 v61, vcc, 0, v69, vcc
	v_add_co_u32_e32 v62, vcc, s42, v68
	s_nop 1
	v_addc_co_u32_e32 v63, vcc, 0, v69, vcc
	v_add_co_u32_e32 v64, vcc, s43, v68
	s_nop 1
	v_addc_co_u32_e32 v65, vcc, 0, v69, vcc
	v_add_co_u32_e32 v66, vcc, s44, v68
	s_nop 1
	v_addc_co_u32_e32 v67, vcc, 0, v69, vcc
	global_load_dword v51, v[52:53], off nt
	s_nop 0
	global_load_dword v52, v[54:55], off nt
	global_load_dword v53, v[56:57], off nt
	s_nop 0
	global_load_dword v54, v[58:59], off nt
	global_load_dword v55, v[60:61], off nt
	global_load_dword v56, v[62:63], off nt
	global_load_dword v57, v[64:65], off nt
	s_nop 0
	global_load_dword v58, v[66:67], off nt
	v_add_co_u32_e32 v60, vcc, s45, v68
	s_nop 1
	v_addc_co_u32_e32 v61, vcc, 0, v69, vcc
	v_add_co_u32_e32 v62, vcc, s46, v68
	s_nop 1
	v_addc_co_u32_e32 v63, vcc, 0, v69, vcc
	v_add_co_u32_e32 v64, vcc, s47, v68
	s_nop 1
	v_addc_co_u32_e32 v65, vcc, 0, v69, vcc
	v_add_co_u32_e32 v66, vcc, s48, v68
	s_nop 1
	v_addc_co_u32_e32 v67, vcc, 0, v69, vcc
	v_add_co_u32_e32 v70, vcc, s49, v68
	s_nop 1
	v_addc_co_u32_e32 v71, vcc, 0, v69, vcc
	v_add_co_u32_e32 v72, vcc, s50, v68
	s_nop 1
	v_addc_co_u32_e32 v73, vcc, 0, v69, vcc
	v_add_co_u32_e32 v74, vcc, s51, v68
	s_nop 1
	v_addc_co_u32_e32 v75, vcc, 0, v69, vcc
	v_add_co_u32_e32 v76, vcc, s52, v68
	s_nop 1
	v_addc_co_u32_e32 v77, vcc, 0, v69, vcc
	global_load_dword v59, v[60:61], off nt
	s_nop 0
	global_load_dword v60, v[62:63], off nt
	global_load_dword v61, v[64:65], off nt
	s_nop 0
	global_load_dword v62, v[66:67], off nt
	global_load_dword v63, v[70:71], off nt
	global_load_dword v64, v[72:73], off nt
	global_load_dword v65, v[74:75], off nt
	s_nop 0
	global_load_dword v66, v[76:77], off nt
	v_add_co_u32_e32 v70, vcc, s53, v68
	s_nop 1
	v_addc_co_u32_e32 v71, vcc, 0, v69, vcc
	v_add_co_u32_e32 v72, vcc, s54, v68
	s_nop 1
	v_addc_co_u32_e32 v73, vcc, 0, v69, vcc
	v_add_co_u32_e32 v74, vcc, s55, v68
	s_nop 1
	v_addc_co_u32_e32 v75, vcc, 0, v69, vcc
	v_add_co_u32_e32 v76, vcc, s56, v68
	s_nop 1
	v_addc_co_u32_e32 v77, vcc, 0, v69, vcc
	v_add_co_u32_e32 v78, vcc, 0xe0000, v68
	s_nop 1
	v_addc_co_u32_e32 v79, vcc, 0, v69, vcc
	v_add_co_u32_e32 v80, vcc, 0xe8000, v68
	s_nop 1
	v_addc_co_u32_e32 v81, vcc, 0, v69, vcc
	v_add_co_u32_e32 v82, vcc, 0xf0000, v68
	s_nop 1
	v_addc_co_u32_e32 v83, vcc, 0, v69, vcc
	v_add_co_u32_e32 v84, vcc, 0xf8000, v68
	s_nop 1
	v_addc_co_u32_e32 v85, vcc, 0, v69, vcc
	global_load_dword v67, v[70:71], off nt
	global_load_dword v68, v[72:73], off nt
	global_load_dword v69, v[74:75], off nt
	s_nop 0
	global_load_dword v70, v[76:77], off nt
	global_load_dword v71, v[78:79], off nt
	global_load_dword v72, v[80:81], off nt
	global_load_dword v73, v[82:83], off nt
	global_load_dword v74, v[84:85], off nt
	s_branch .LBB0_2052

; __device__ __forceinline__ float wave_max(float v) { v = dpp_max16(v); return fmaxf(fmaxf(rdlane(v, 0), rdlane(v, 16)), fmaxf(rdlane(v, 32), rdlane(v, 48))); }
; __device__ __forceinline__ unsigned fp6_code(float y) {
;     const float a = fminf(fabsf(y), 7.5f);
;     const int m = a < 2.0f ? (int)rintf(a * 8.0f) : (a < 4.0f ? 16 + (int)rintf((a - 2.0f) * 4.0f) : 24 + (int)rintf((a - 4.0f) * 2.0f));
;     return (unsigned)m | (y < 0.f ? 32u : 0u);
; __device__ __forceinline__ void quant_rows_fp6(const float* src, unsigned char* dst, float* scales, int nrows, int gw, int ngw, int lane) {
;     for (int r = gw; r < nrows; r += ngw) {
;         const f32x4* s4 = (const f32x4*)(src + (size_t)r * D_) + lane; f32x4 v[16]; float m = 0.f;
; #pragma unroll
;         for (int j = 0; j < 16; ++j) { v[j] = s4[64 * j]; m = fmaxf(fmaxf(m, fmaxf(fabsf(v[j].x), fabsf(v[j].y))), fmaxf(fabsf(v[j].z), fabsf(v[j].w))); }
;         m = wave_max(m); const float inv = m > 0.f ? 7.5f / m : 0.f;
.LBB0_2168:
	v_add_co_u32_e32 v2, vcc, s28, v68
	global_load_dwordx4 v[62:65], v[68:69], off nt
	global_load_dwordx4 v[58:61], v[68:69], off offset:1024 nt
	global_load_dwordx4 v[54:57], v[68:69], off offset:2048 nt
	global_load_dwordx4 v[50:53], v[68:69], off offset:3072 nt
	v_addc_co_u32_e32 v3, vcc, 0, v69, vcc
	global_load_dwordx4 v[46:49], v[2:3], off offset:-4096 nt
	v_add_co_u32_e32 v4, vcc, s13, v68
	s_waitcnt vmcnt(4)
	v_max_f32_e64 v71, |v63|, |v63|
	v_addc_co_u32_e32 v5, vcc, 0, v69, vcc
	global_load_dwordx4 v[42:45], v[4:5], off offset:1024 nt
	global_load_dwordx4 v[38:41], v[4:5], off offset:2048 nt
	global_load_dwordx4 v[34:37], v[4:5], off offset:3072 nt
	global_load_dwordx4 v[30:33], v[2:3], off nt
	global_load_dwordx4 v[26:29], v[2:3], off offset:1024 nt
	global_load_dwordx4 v[22:25], v[2:3], off offset:2048 nt
	v_add_co_u32_e32 v72, vcc, s29, v68
	v_max_f32_e64 v74, |v64|, |v64|
	s_nop 0
	v_addc_co_u32_e32 v73, vcc, 0, v69, vcc
	global_load_dwordx4 v[18:21], v[2:3], off offset:3072 nt
	global_load_dwordx4 v[14:17], v[72:73], off nt
	global_load_dwordx4 v[10:13], v[72:73], off offset:1024 nt
	global_load_dwordx4 v[6:9], v[72:73], off offset:2048 nt
	s_nop 0
	global_load_dwordx4 v[2:5], v[72:73], off offset:3072 nt
	v_max_f32_e64 v72, |v62|, |v62|
	v_max_f32_e64 v73, |v65|, |v65|
	s_waitcnt vmcnt(14)
	v_max_f32_e64 v75, |v59|, |v59|
	v_max_f32_e64 v76, |v58|, |v58|
	v_max_f32_e64 v77, |v61|, |v61|
	v_max_f32_e64 v78, |v60|, |v60|
	v_max_f32_e32 v71, v72, v71
	v_max_f32_e32 v72, v74, v73
	s_waitcnt vmcnt(13)
	v_max_f32_e64 v79, |v55|, |v55|
	v_max_f32_e64 v80, |v54|, |v54|
	v_max_f32_e64 v81, |v57|, |v57|
	v_max_f32_e64 v82, |v56|, |v56|
	v_max_f32_e32 v73, v76, v75
	v_max_f32_e32 v74, v78, v77
	v_max3_f32 v71, v71, 0, v72
	s_waitcnt vmcnt(12)
	v_max_f32_e64 v83, |v51|, |v51|
	v_max_f32_e64 v84, |v50|, |v50|
	v_max_f32_e64 v85, |v53|, |v53|
	v_max_f32_e64 v86, |v52|, |v52|
	v_max_f32_e32 v75, v80, v79
	v_max_f32_e32 v76, v82, v81
	v_max3_f32 v71, v71, v73, v74
	v_max_f32_e32 v77, v84, v83
	v_max_f32_e32 v78, v86, v85
	s_waitcnt vmcnt(11)
	v_max_f32_e64 v79, |v47|, |v47|
	v_max_f32_e64 v80, |v46|, |v46|
	v_max_f32_e64 v81, |v49|, |v49|
	v_max_f32_e64 v82, |v48|, |v48|
	v_max3_f32 v71, v71, v75, v76
	v_max_f32_e32 v72, v80, v79
	v_max_f32_e32 v79, v82, v81
	v_max3_f32 v71, v71, v77, v78
	v_max3_f32 v71, v71, v72, v79
	s_waitcnt vmcnt(10)
	v_max_f32_e64 v83, |v43|, |v43|
	v_max_f32_e64 v84, |v42|, |v42|
	v_max_f32_e64 v85, |v45|, |v45|
	v_max_f32_e64 v86, |v44|, |v44|
	s_waitcnt vmcnt(9)
	v_max_f32_e64 v87, |v39|, |v39|
	v_max_f32_e64 v88, |v38|, |v38|
	v_max_f32_e64 v89, |v41|, |v41|
	v_max_f32_e64 v90, |v40|, |v40|
	v_max_f32_e32 v80, v84, v83
	v_max_f32_e32 v81, v86, v85
	s_waitcnt vmcnt(8)
	v_max_f32_e64 v91, |v35|, |v35|
	v_max_f32_e64 v92, |v34|, |v34|
	v_max_f32_e64 v93, |v37|, |v37|
	v_max_f32_e64 v94, |v36|, |v36|
	v_max_f32_e32 v82, v88, v87
	v_max_f32_e32 v83, v90, v89
	v_max3_f32 v71, v71, v80, v81
	s_waitcnt vmcnt(7)
	v_max_f32_e64 v95, |v31|, |v31|
	v_max_f32_e64 v96, |v30|, |v30|
	v_max_f32_e64 v97, |v33|, |v33|
	v_max_f32_e64 v98, |v32|, |v32|
	v_max_f32_e32 v84, v92, v91
	v_max_f32_e32 v85, v94, v93
	v_max3_f32 v71, v71, v82, v83
	s_waitcnt vmcnt(6)
	v_max_f32_e64 v72, |v27|, |v27|
	v_max_f32_e64 v73, |v26|, |v26|
	v_max_f32_e32 v86, v96, v95
	v_max_f32_e32 v87, v98, v97
	v_max3_f32 v71, v71, v84, v85
	v_max_f32_e32 v72, v73, v72
	v_max_f32_e64 v73, |v29|, |v29|
	v_max_f32_e64 v74, |v28|, |v28|
	v_max3_f32 v71, v71, v86, v87
	v_max_f32_e32 v73, v74, v73
	v_max3_f32 v71, v71, v72, v73
	s_waitcnt vmcnt(5)
	v_max_f32_e64 v72, |v23|, |v23|
	v_max_f32_e64 v73, |v22|, |v22|
	v_max_f32_e32 v72, v73, v72
	v_max_f32_e64 v73, |v25|, |v25|
	v_max_f32_e64 v74, |v24|, |v24|
	v_max_f32_e32 v73, v74, v73
	v_max3_f32 v71, v71, v72, v73
	s_waitcnt vmcnt(4)
	v_max_f32_e64 v72, |v19|, |v19|
	v_max_f32_e64 v73, |v18|, |v18|
	v_max_f32_e32 v72, v73, v72
	v_max_f32_e64 v73, |v21|, |v21|
	v_max_f32_e64 v74, |v20|, |v20|
	v_max_f32_e32 v73, v74, v73
	v_max3_f32 v71, v71, v72, v73
	s_waitcnt vmcnt(3)
	v_max_f32_e64 v72, |v15|, |v15|
	v_max_f32_e64 v73, |v14|, |v14|
	v_max_f32_e32 v72, v73, v72
	v_max_f32_e64 v73, |v17|, |v17|
	v_max_f32_e64 v74, |v16|, |v16|
	v_max_f32_e32 v73, v74, v73
	v_max3_f32 v71, v71, v72, v73
	s_waitcnt vmcnt(2)
	v_max_f32_e64 v72, |v11|, |v11|
	v_max_f32_e64 v73, |v10|, |v10|
	v_max_f32_e32 v72, v73, v72
	v_max_f32_e64 v73, |v13|, |v13|
	v_max_f32_e64 v74, |v12|, |v12|
	v_max_f32_e32 v73, v74, v73
	v_max3_f32 v71, v71, v72, v73
	s_waitcnt vmcnt(1)
	v_max_f32_e64 v72, |v7|, |v7|
	v_max_f32_e64 v73, |v6|, |v6|
	v_max_f32_e32 v72, v73, v72
	v_max_f32_e64 v73, |v9|, |v9|
	v_max_f32_e64 v74, |v8|, |v8|
	v_max_f32_e32 v73, v74, v73
	v_max3_f32 v71, v71, v72, v73
	s_waitcnt vmcnt(0)
	v_max_f32_e64 v72, |v3|, |v3|
	v_max_f32_e64 v73, |v2|, |v2|
	v_max_f32_e32 v72, v73, v72
	v_max_f32_e64 v73, |v5|, |v5|
	v_max_f32_e64 v74, |v4|, |v4|
	v_max_f32_e32 v73, v74, v73
	v_max3_f32 v71, v71, v72, v73
	v_mov_b32_e32 v72, 0
	s_nop 1
	v_mov_b32_dpp v72, v71 quad_perm:[1,0,3,2] row_mask:0xf bank_mask:0xf
	v_max_f32_e32 v72, v72, v72
	v_max_f32_e32 v71, v71, v72
	v_mov_b32_e32 v72, 0
	s_nop 1
	v_mov_b32_dpp v72, v71 quad_perm:[2,3,0,1] row_mask:0xf bank_mask:0xf
	v_max_f32_e32 v72, v72, v72
	v_max_f32_e32 v71, v71, v72
	v_mov_b32_e32 v72, 0
	s_nop 1
	v_mov_b32_dpp v72, v71 row_half_mirror row_mask:0xf bank_mask:0xf
	v_max_f32_e32 v72, v72, v72
	v_max_f32_e32 v71, v71, v72
	v_mov_b32_e32 v72, 0
	s_nop 1
	v_mov_b32_dpp v72, v71 row_mirror row_mask:0xf bank_mask:0xf
	v_max_f32_e32 v72, v72, v72
	v_max_f32_e32 v71, v71, v72
	s_nop 0
	v_readlane_b32 s22, v71, 32
	v_readlane_b32 s23, v71, 48
	v_readlane_b32 s20, v71, 0
	v_readlane_b32 s21, v71, 16
	v_max_f32_e64 v71, s23, s23
	v_max_f32_e64 v72, s22, s22
	v_max_f32_e32 v71, v72, v71
	v_mov_b32_e32 v72, s21
	v_max3_f32 v71, s20, v72, v71
	v_div_scale_f32 v72, s[20:21], v71, v71, s30
	v_rcp_f32_e32 v73, v72
	s_nop 0
	v_fma_f32 v74, -v72, v73, 1.0
	v_fmac_f32_e32 v73, v74, v73
	v_div_scale_f32 v74, vcc, s30, v71, s30
	v_mul_f32_e32 v75, v74, v73
	v_fma_f32 v76, -v72, v75, v74
	v_fmac_f32_e32 v75, v76, v73
	v_fma_f32 v72, -v72, v75, v74
	v_div_fmas_f32 v72, v72, v73, v75
	v_div_fixup_f32 v72, v72, v71, s30
	v_cmp_lt_f32_e32 vcc, 0, v71
	s_nop 1
	v_cndmask_b32_e32 v72, 0, v72, vcc
	v_mul_f32_e32 v62, v62, v72
	v_min_f32_e64 v74, |v62|, s30
	v_cmp_ngt_f32_e32 vcc, 2.0, v74
	s_and_saveexec_b64 s[20:21], vcc
	s_xor_b64 s[20:21], exec, s[20:21]
	s_cbranch_execz .LBB0_2174
	v_cmp_ngt_f32_e32 vcc, 4.0, v74
	s_and_saveexec_b64 s[22:23], vcc
	s_xor_b64 s[22:23], exec, s[22:23]
	v_add_f32_e32 v73, -4.0, v74
	v_add_f32_e32 v73, v73, v73
	v_rndne_f32_e32 v73, v73
	v_cvt_i32_f32_e32 v73, v73
	v_add_u32_e32 v73, 24, v73
	s_andn2_saveexec_b64 s[22:23], s[22:23]
	v_add_f32_e32 v73, -2.0, v74
	v_mul_f32_e32 v73, 4.0, v73
	v_rndne_f32_e32 v73, v73
	v_cvt_i32_f32_e32 v73, v73
	v_add_u32_e32 v73, 16, v73
	s_or_b64 exec, exec, s[22:23]
